# stack of two individually-neutral edits: fq+-2 screening after the output stores + SGPR-base DMA addressing in the GEMM loop (no per-trip 64-bit VALU address bumps)
# speedup vs baseline: 1.0106x; 1.0018x over previous
_Z8gemm_qkvPKDF16_S0_PKfPDF16_S3_S3_Pj:
	v_readfirstlane_b32 s13, v0
	s_lshr_b32 s8, s13, 6
	v_bfe_u32 v2, v0, 3, 3
	s_load_dwordx4 s[4:7], s[0:1], 0x0
	v_lshl_or_b32 v6, s8, 3, v2
	v_lshrrev_b32_e32 v2, 1, v6
	s_mul_i32 s16, s3, 0xc0
	v_xor_b32_e32 v4, v2, v0
	v_add_u32_e32 v2, s16, v6
	v_ashrrev_i32_e32 v3, 31, v2
	s_bfe_u32 s15, s13, 0x20006
	v_lshlrev_b64 v[2:3], 11, v[2:3]
	v_lshlrev_b32_e32 v4, 4, v4
	s_mul_i32 s10, s2, 0xc0
	s_mul_i32 s2, s15, 48
	s_waitcnt lgkmcnt(0)
	v_lshl_add_u64 v[2:3], s[4:5], 0, v[2:3]
	v_and_b32_e32 v4, 0x70, v4
	v_mov_b32_e32 v5, 0
	s_add_i32 s17, s2, s10
	v_lshl_add_u64 v[218:219], v[2:3], 0, v[4:5]
	v_add_u32_e32 v2, s10, v6
	s_lshl_b32 s8, s8, 10
	v_ashrrev_i32_e32 v3, 31, v2
	s_cmp_lg_u32 0x400, -1
	v_lshlrev_b64 v[2:3], 11, v[2:3]
	s_cselect_b32 s4, 0x400, 0
	v_lshl_add_u64 v[2:3], s[6:7], 0, v[2:3]
	s_add_i32 s11, s8, s4
	s_mov_b32 s4, m0
	s_mov_b32 m0, s11
	s_nop 0
	global_load_lds_dwordx4 v[218:219], off
	s_mov_b32 m0, s4
	v_lshl_add_u64 v[220:221], v[2:3], 0, v[4:5]
	s_add_i32 s4, s11, 0x6000
	s_mov_b32 s5, m0
	s_mov_b32 m0, s4
	s_nop 0
	global_load_lds_dwordx4 v[220:221], off
	s_mov_b32 m0, s5
	s_mov_b64 s[4:5], 0x20000
	v_lshl_add_u64 v[222:223], v[218:219], 0, s[4:5]
	s_add_i32 s9, s11, 0x2000
	s_mov_b32 s6, m0
	s_mov_b32 m0, s9
	s_nop 0
	global_load_lds_dwordx4 v[222:223], off
	s_mov_b32 m0, s6
	v_lshl_add_u64 v[224:225], v[220:221], 0, s[4:5]
	s_add_i32 s4, s11, 0x8000
	s_mov_b32 s5, m0
	s_mov_b32 m0, s4
	s_nop 0
	global_load_lds_dwordx4 v[224:225], off
	s_mov_b32 m0, s5
	s_mov_b64 s[4:5], 0x40000
	v_lshl_add_u64 v[226:227], v[218:219], 0, s[4:5]
	s_add_i32 s12, s11, 0x4000
	s_mov_b32 s6, m0
	s_mov_b32 m0, s12
	s_nop 0
	global_load_lds_dwordx4 v[226:227], off
	s_mov_b32 m0, s6
	v_lshl_add_u64 v[228:229], v[220:221], 0, s[4:5]
	s_add_i32 s4, s11, 0xa000
	s_mov_b32 s5, m0
	s_mov_b32 m0, s4
	s_nop 0
	global_load_lds_dwordx4 v[228:229], off
	s_mov_b32 m0, s5
	s_cmpk_gt_i32 s17, 0x7d0
	s_cselect_b64 s[4:5], -1, 0
	s_lshr_b32 s14, s13, 8
	s_mul_i32 s6, s14, 0x3000
	s_add_i32 s13, s6, 0x400
	s_mov_b64 s[6:7], 0x80
	s_add_i32 s18, s11, 0xc000
	v_lshl_add_u64 v[2:3], v[218:219], 0, s[6:7]
	s_mov_b32 s30, m0
	s_mov_b32 m0, s18
	s_nop 0
	global_load_lds_dwordx4 v[2:3], off
	s_mov_b32 m0, s30
	s_add_i32 s19, s11, 0x12000
	v_lshl_add_u64 v[2:3], v[220:221], 0, s[6:7]
	s_mov_b32 s6, m0
	s_mov_b32 m0, s19
	s_nop 0
	global_load_lds_dwordx4 v[2:3], off
	s_mov_b32 m0, s6
	s_mov_b64 s[6:7], 0x20080
	s_add_i32 s20, s11, 0xe000
	v_lshl_add_u64 v[2:3], v[218:219], 0, s[6:7]
	s_mov_b32 s18, m0
	s_mov_b32 m0, s20
	s_nop 0
	global_load_lds_dwordx4 v[2:3], off
	s_mov_b32 m0, s18
	s_add_i32 s21, s11, 0x14000
	v_lshl_add_u64 v[2:3], v[220:221], 0, s[6:7]
	s_mov_b32 s6, m0
	s_mov_b32 m0, s21
	s_nop 0
	global_load_lds_dwordx4 v[2:3], off
	s_mov_b32 m0, s6
	s_mov_b64 s[6:7], 0x40080
	v_lshl_add_u64 v[2:3], v[218:219], 0, s[6:7]
	s_add_i32 s22, s11, 0x10000
	s_mov_b32 s18, m0
	s_mov_b32 m0, s22
	s_nop 0
	global_load_lds_dwordx4 v[2:3], off
	s_mov_b32 m0, s18
	v_lshl_add_u64 v[2:3], v[220:221], 0, s[6:7]
	v_and_b32_e32 v1, 15, v0
	v_bfe_u32 v231, v0, 4, 2
	s_add_i32 s23, s11, 0x16000
	s_mov_b32 s6, m0
	s_mov_b32 m0, s23
	s_nop 0
	global_load_lds_dwordx4 v[2:3], off
	s_mov_b32 m0, s6
	v_lshrrev_b32_e32 v3, 1, v0
	v_lshlrev_b32_e32 v2, 7, v1
	v_bfe_u32 v4, v0, 1, 3
	v_bitop3_b32 v3, v231, v3, 7 bitop3:0x78
	v_lshl_or_b32 v238, v3, 4, v2
	v_bitop3_b32 v3, v231, v4, 4 bitop3:0x36
	v_lshl_or_b32 v240, v3, 4, v2
	s_mulk_i32 s15, 0x1800
	s_addk_i32 s15, 0x6400
	v_add_u32_e32 v158, s13, v238
	v_add_u32_e32 v160, s13, v240
	v_add_u32_e32 v162, s15, v238
	v_add_u32_e32 v164, s15, v240
	s_load_dwordx4 s[28:31], s[0:1], 0x0
	s_load_dwordx2 s[24:25], s[0:1], 0x10
	s_waitcnt lgkmcnt(0)
	v_subrev_u32_e32 v166, s28, v218
	v_subrev_u32_e32 v167, s28, v222
	v_subrev_u32_e32 v168, s28, v226
	v_subrev_u32_e32 v169, s30, v220
	v_subrev_u32_e32 v170, s30, v224
	v_subrev_u32_e32 v171, s30, v228
	s_add_u32 m0, s11, 0x17f00
	s_nop 0
	global_load_lds_dwordx4 v166, s[28:29] offset:256
	s_add_u32 m0, s11, 0x19f00
	s_nop 0
	global_load_lds_dwordx4 v167, s[28:29] offset:256
	s_add_u32 m0, s11, 0x1bf00
	s_nop 0
	global_load_lds_dwordx4 v168, s[28:29] offset:256
	s_add_u32 s28, s28, 0x180
	s_addc_u32 s29, s29, 0
	s_add_u32 s30, s30, 0x180
	s_addc_u32 s31, s31, 0
	v_add_u32_e32 v159, 0x18000, v158
	v_add_u32_e32 v161, 0x18000, v160
	v_add_u32_e32 v163, 0x18000, v162
	v_add_u32_e32 v165, 0x18000, v164
	v_mov_b32_e32 v82, 0
	v_mov_b32_e32 v83, 0
	v_mov_b32_e32 v84, 0
	v_mov_b32_e32 v85, 0
	v_mov_b32_e32 v58, 0
	v_mov_b32_e32 v59, 0
	v_mov_b32_e32 v60, 0
	v_mov_b32_e32 v61, 0
	v_mov_b32_e32 v14, 0
	v_mov_b32_e32 v15, 0
	v_mov_b32_e32 v16, 0
	v_mov_b32_e32 v17, 0
	v_mov_b32_e32 v78, 0
	v_mov_b32_e32 v79, 0
	v_mov_b32_e32 v80, 0
	v_mov_b32_e32 v81, 0
	v_mov_b32_e32 v22, 0
	v_mov_b32_e32 v23, 0
	v_mov_b32_e32 v24, 0
	v_mov_b32_e32 v25, 0
	v_mov_b32_e32 v30, 0
	v_mov_b32_e32 v31, 0
	v_mov_b32_e32 v32, 0
	v_mov_b32_e32 v33, 0
	v_mov_b32_e32 v74, 0
	v_mov_b32_e32 v75, 0
	v_mov_b32_e32 v76, 0
	v_mov_b32_e32 v77, 0
	v_mov_b32_e32 v18, 0
	v_mov_b32_e32 v19, 0
	v_mov_b32_e32 v20, 0
	v_mov_b32_e32 v21, 0
	v_mov_b32_e32 v26, 0
	v_mov_b32_e32 v27, 0
	v_mov_b32_e32 v28, 0
	v_mov_b32_e32 v29, 0
	v_mov_b32_e32 v70, 0
	v_mov_b32_e32 v71, 0
	v_mov_b32_e32 v72, 0
	v_mov_b32_e32 v73, 0
	v_mov_b32_e32 v46, 0
	v_mov_b32_e32 v47, 0
	v_mov_b32_e32 v48, 0
	v_mov_b32_e32 v49, 0
	v_mov_b32_e32 v240, 0
	v_mov_b32_e32 v241, 0
	v_mov_b32_e32 v242, 0
	v_mov_b32_e32 v243, 0
	v_mov_b32_e32 v66, 0
	v_mov_b32_e32 v67, 0
	v_mov_b32_e32 v68, 0
	v_mov_b32_e32 v69, 0
	v_mov_b32_e32 v42, 0
	v_mov_b32_e32 v43, 0
	v_mov_b32_e32 v44, 0
	v_mov_b32_e32 v45, 0
	v_mov_b32_e32 v236, 0
	v_mov_b32_e32 v237, 0
	v_mov_b32_e32 v238, 0
	v_mov_b32_e32 v239, 0
	v_mov_b32_e32 v62, 0
	v_mov_b32_e32 v63, 0
	v_mov_b32_e32 v64, 0
	v_mov_b32_e32 v65, 0
	v_mov_b32_e32 v38, 0
	v_mov_b32_e32 v39, 0
	v_mov_b32_e32 v40, 0
	v_mov_b32_e32 v41, 0
	v_mov_b32_e32 v34, 0
	v_mov_b32_e32 v35, 0
	v_mov_b32_e32 v36, 0
	v_mov_b32_e32 v37, 0
	s_not_b64 s[6:7], s[4:5]
	s_mov_b32 s22, 4
	s_waitcnt vmcnt(9) lgkmcnt(0)
	s_barrier
	ds_read_b128 v[134:137], v162
	ds_read_b128 v[138:141], v162 offset:2048
	ds_read_b128 v[142:145], v162 offset:4096
	ds_read_b128 v[86:89], v158
	ds_read_b128 v[90:93], v158 offset:2048
	ds_read_b128 v[94:97], v158 offset:4096
	ds_read_b128 v[98:101], v158 offset:6144
	ds_read_b128 v[102:105], v158 offset:8192
	ds_read_b128 v[106:109], v158 offset:10240
	ds_read_b128 v[110:113], v160
	ds_read_b128 v[114:117], v160 offset:2048
	ds_read_b128 v[118:121], v160 offset:4096
	ds_read_b128 v[122:125], v160 offset:6144
	ds_read_b128 v[126:129], v160 offset:8192
	ds_read_b128 v[130:133], v160 offset:10240
	ds_read_b128 v[146:149], v164
	ds_read_b128 v[150:153], v164 offset:2048
	ds_read_b128 v[154:157], v164 offset:4096
	s_and_b64 vcc, exec, s[4:5]
	s_cbranch_vccnz .Lgemm_N_loop
.Lgemm_T_loop:
	s_waitcnt lgkmcnt(9)
	s_add_u32 m0, s11, 0x1e080
	v_mfma_f32_16x16x32_f16 v[82:85], v[134:137], v[86:89], v[82:85]
	global_load_lds_dwordx4 v169, s[30:31] offset:-128
	v_mfma_f32_16x16x32_f16 v[58:61], v[138:141], v[86:89], v[58:61]
	v_mfma_f32_16x16x32_f16 v[14:17], v[142:145], v[86:89], v[14:17]
	v_mfma_f32_16x16x32_f16 v[78:81], v[134:137], v[90:93], v[78:81]
	v_mfma_f32_16x16x32_f16 v[22:25], v[138:141], v[90:93], v[22:25]
	v_mfma_f32_16x16x32_f16 v[30:33], v[142:145], v[90:93], v[30:33]
	s_add_u32 m0, s11, 0x20080
	v_mfma_f32_16x16x32_f16 v[74:77], v[134:137], v[94:97], v[74:77]
	global_load_lds_dwordx4 v170, s[30:31] offset:-128
	v_mfma_f32_16x16x32_f16 v[18:21], v[138:141], v[94:97], v[18:21]
	v_mfma_f32_16x16x32_f16 v[26:29], v[142:145], v[94:97], v[26:29]
	v_mfma_f32_16x16x32_f16 v[70:73], v[134:137], v[98:101], v[70:73]
	v_mfma_f32_16x16x32_f16 v[46:49], v[138:141], v[98:101], v[46:49]
	v_mfma_f32_16x16x32_f16 v[240:243], v[142:145], v[98:101], v[240:243]
	s_add_u32 m0, s11, 0x22080
	v_mfma_f32_16x16x32_f16 v[66:69], v[134:137], v[102:105], v[66:69]
	global_load_lds_dwordx4 v171, s[30:31] offset:-128
	v_mfma_f32_16x16x32_f16 v[42:45], v[138:141], v[102:105], v[42:45]
	v_mfma_f32_16x16x32_f16 v[236:239], v[142:145], v[102:105], v[236:239]
	v_mfma_f32_16x16x32_f16 v[62:65], v[134:137], v[106:109], v[62:65]
	v_mfma_f32_16x16x32_f16 v[38:41], v[138:141], v[106:109], v[38:41]
	v_mfma_f32_16x16x32_f16 v[34:37], v[142:145], v[106:109], v[34:37]
	s_waitcnt vmcnt(6) lgkmcnt(0)
	s_barrier
	s_add_u32 m0, s11, 0x0
	ds_read_b128 v[134:137], v162 offset:49152
	global_load_lds_dwordx4 v166, s[28:29]
	v_mfma_f32_16x16x32_f16 v[82:85], v[146:149], v[110:113], v[82:85]
	ds_read_b128 v[138:141], v162 offset:51200
	v_mfma_f32_16x16x32_f16 v[58:61], v[150:153], v[110:113], v[58:61]
	ds_read_b128 v[142:145], v162 offset:53248
	v_mfma_f32_16x16x32_f16 v[14:17], v[154:157], v[110:113], v[14:17]
	ds_read_b128 v[86:89], v158 offset:49152
	v_mfma_f32_16x16x32_f16 v[78:81], v[146:149], v[114:117], v[78:81]
	ds_read_b128 v[90:93], v158 offset:51200
	v_mfma_f32_16x16x32_f16 v[22:25], v[150:153], v[114:117], v[22:25]
	ds_read_b128 v[94:97], v158 offset:53248
	v_mfma_f32_16x16x32_f16 v[30:33], v[154:157], v[114:117], v[30:33]
	s_add_u32 m0, s11, 0x2000
	ds_read_b128 v[98:101], v158 offset:55296
	global_load_lds_dwordx4 v167, s[28:29]
	v_mfma_f32_16x16x32_f16 v[74:77], v[146:149], v[118:121], v[74:77]
	ds_read_b128 v[102:105], v158 offset:57344
	v_mfma_f32_16x16x32_f16 v[18:21], v[150:153], v[118:121], v[18:21]
	ds_read_b128 v[106:109], v158 offset:59392
	v_mfma_f32_16x16x32_f16 v[26:29], v[154:157], v[118:121], v[26:29]
	ds_read_b128 v[110:113], v160 offset:49152
	v_mfma_f32_16x16x32_f16 v[70:73], v[146:149], v[122:125], v[70:73]
	ds_read_b128 v[114:117], v160 offset:51200
	v_mfma_f32_16x16x32_f16 v[46:49], v[150:153], v[122:125], v[46:49]
	v_mfma_f32_16x16x32_f16 v[240:243], v[154:157], v[122:125], v[240:243]
	s_add_u32 m0, s11, 0x4000
	ds_read_b128 v[118:121], v160 offset:53248
	global_load_lds_dwordx4 v168, s[28:29]
	v_mfma_f32_16x16x32_f16 v[66:69], v[146:149], v[126:129], v[66:69]
	ds_read_b128 v[122:125], v160 offset:55296
	v_mfma_f32_16x16x32_f16 v[42:45], v[150:153], v[126:129], v[42:45]
	v_mfma_f32_16x16x32_f16 v[236:239], v[154:157], v[126:129], v[236:239]
	ds_read_b128 v[126:129], v160 offset:57344
	v_mfma_f32_16x16x32_f16 v[62:65], v[146:149], v[130:133], v[62:65]
	v_mfma_f32_16x16x32_f16 v[38:41], v[150:153], v[130:133], v[38:41]
	v_mfma_f32_16x16x32_f16 v[34:37], v[154:157], v[130:133], v[34:37]
	ds_read_b128 v[130:133], v160 offset:59392
	ds_read_b128 v[146:149], v164 offset:49152
	ds_read_b128 v[150:153], v164 offset:51200
	ds_read_b128 v[154:157], v164 offset:53248
	s_waitcnt lgkmcnt(9)
	s_add_u32 m0, s11, 0x6000
	v_mfma_f32_16x16x32_f16 v[82:85], v[134:137], v[86:89], v[82:85]
	global_load_lds_dwordx4 v169, s[30:31]
	v_mfma_f32_16x16x32_f16 v[58:61], v[138:141], v[86:89], v[58:61]
	v_mfma_f32_16x16x32_f16 v[14:17], v[142:145], v[86:89], v[14:17]
	v_mfma_f32_16x16x32_f16 v[78:81], v[134:137], v[90:93], v[78:81]
	v_mfma_f32_16x16x32_f16 v[22:25], v[138:141], v[90:93], v[22:25]
	v_mfma_f32_16x16x32_f16 v[30:33], v[142:145], v[90:93], v[30:33]
	s_add_u32 m0, s11, 0x8000
	v_mfma_f32_16x16x32_f16 v[74:77], v[134:137], v[94:97], v[74:77]
	global_load_lds_dwordx4 v170, s[30:31]
	v_mfma_f32_16x16x32_f16 v[18:21], v[138:141], v[94:97], v[18:21]
	v_mfma_f32_16x16x32_f16 v[26:29], v[142:145], v[94:97], v[26:29]
	v_mfma_f32_16x16x32_f16 v[70:73], v[134:137], v[98:101], v[70:73]
	v_mfma_f32_16x16x32_f16 v[46:49], v[138:141], v[98:101], v[46:49]
	v_mfma_f32_16x16x32_f16 v[240:243], v[142:145], v[98:101], v[240:243]
	s_add_u32 m0, s11, 0xa000
	v_mfma_f32_16x16x32_f16 v[66:69], v[134:137], v[102:105], v[66:69]
	global_load_lds_dwordx4 v171, s[30:31]
	v_mfma_f32_16x16x32_f16 v[42:45], v[138:141], v[102:105], v[42:45]
	v_mfma_f32_16x16x32_f16 v[236:239], v[142:145], v[102:105], v[236:239]
	v_mfma_f32_16x16x32_f16 v[62:65], v[134:137], v[106:109], v[62:65]
	v_mfma_f32_16x16x32_f16 v[38:41], v[138:141], v[106:109], v[38:41]
	v_mfma_f32_16x16x32_f16 v[34:37], v[142:145], v[106:109], v[34:37]
	s_waitcnt vmcnt(6) lgkmcnt(0)
	s_barrier
	s_add_u32 m0, s11, 0xbf80
	ds_read_b128 v[134:137], v163
	global_load_lds_dwordx4 v166, s[28:29] offset:128
	v_mfma_f32_16x16x32_f16 v[82:85], v[146:149], v[110:113], v[82:85]
	ds_read_b128 v[138:141], v163 offset:2048
	v_mfma_f32_16x16x32_f16 v[58:61], v[150:153], v[110:113], v[58:61]
	ds_read_b128 v[142:145], v163 offset:4096
	v_mfma_f32_16x16x32_f16 v[14:17], v[154:157], v[110:113], v[14:17]
	ds_read_b128 v[86:89], v159
	v_mfma_f32_16x16x32_f16 v[78:81], v[146:149], v[114:117], v[78:81]
	ds_read_b128 v[90:93], v159 offset:2048
	v_mfma_f32_16x16x32_f16 v[22:25], v[150:153], v[114:117], v[22:25]
	ds_read_b128 v[94:97], v159 offset:4096
	v_mfma_f32_16x16x32_f16 v[30:33], v[154:157], v[114:117], v[30:33]
	s_add_u32 m0, s11, 0xdf80
	ds_read_b128 v[98:101], v159 offset:6144
	global_load_lds_dwordx4 v167, s[28:29] offset:128
	v_mfma_f32_16x16x32_f16 v[74:77], v[146:149], v[118:121], v[74:77]
	ds_read_b128 v[102:105], v159 offset:8192
	v_mfma_f32_16x16x32_f16 v[18:21], v[150:153], v[118:121], v[18:21]
	ds_read_b128 v[106:109], v159 offset:10240
	v_mfma_f32_16x16x32_f16 v[26:29], v[154:157], v[118:121], v[26:29]
	ds_read_b128 v[110:113], v161
	v_mfma_f32_16x16x32_f16 v[70:73], v[146:149], v[122:125], v[70:73]
	ds_read_b128 v[114:117], v161 offset:2048
	v_mfma_f32_16x16x32_f16 v[46:49], v[150:153], v[122:125], v[46:49]
	v_mfma_f32_16x16x32_f16 v[240:243], v[154:157], v[122:125], v[240:243]
	s_add_u32 m0, s11, 0xff80
	ds_read_b128 v[118:121], v161 offset:4096
	global_load_lds_dwordx4 v168, s[28:29] offset:128
	v_mfma_f32_16x16x32_f16 v[66:69], v[146:149], v[126:129], v[66:69]
	ds_read_b128 v[122:125], v161 offset:6144
	v_mfma_f32_16x16x32_f16 v[42:45], v[150:153], v[126:129], v[42:45]
	v_mfma_f32_16x16x32_f16 v[236:239], v[154:157], v[126:129], v[236:239]
	ds_read_b128 v[126:129], v161 offset:8192
	v_mfma_f32_16x16x32_f16 v[62:65], v[146:149], v[130:133], v[62:65]
	v_mfma_f32_16x16x32_f16 v[38:41], v[150:153], v[130:133], v[38:41]
	v_mfma_f32_16x16x32_f16 v[34:37], v[154:157], v[130:133], v[34:37]
	ds_read_b128 v[130:133], v161 offset:10240
	ds_read_b128 v[146:149], v165
	ds_read_b128 v[150:153], v165 offset:2048
	ds_read_b128 v[154:157], v165 offset:4096
	s_waitcnt lgkmcnt(9)
	s_add_u32 m0, s11, 0x11f80
	v_mfma_f32_16x16x32_f16 v[82:85], v[134:137], v[86:89], v[82:85]
	global_load_lds_dwordx4 v169, s[30:31] offset:128
	v_mfma_f32_16x16x32_f16 v[58:61], v[138:141], v[86:89], v[58:61]
	v_mfma_f32_16x16x32_f16 v[14:17], v[142:145], v[86:89], v[14:17]
	v_mfma_f32_16x16x32_f16 v[78:81], v[134:137], v[90:93], v[78:81]
	v_mfma_f32_16x16x32_f16 v[22:25], v[138:141], v[90:93], v[22:25]
	v_mfma_f32_16x16x32_f16 v[30:33], v[142:145], v[90:93], v[30:33]
	s_add_u32 m0, s11, 0x13f80
	v_mfma_f32_16x16x32_f16 v[74:77], v[134:137], v[94:97], v[74:77]
	global_load_lds_dwordx4 v170, s[30:31] offset:128
	v_mfma_f32_16x16x32_f16 v[18:21], v[138:141], v[94:97], v[18:21]
	v_mfma_f32_16x16x32_f16 v[26:29], v[142:145], v[94:97], v[26:29]
	v_mfma_f32_16x16x32_f16 v[70:73], v[134:137], v[98:101], v[70:73]
	v_mfma_f32_16x16x32_f16 v[46:49], v[138:141], v[98:101], v[46:49]
	v_mfma_f32_16x16x32_f16 v[240:243], v[142:145], v[98:101], v[240:243]
	s_add_u32 m0, s11, 0x15f80
	v_mfma_f32_16x16x32_f16 v[66:69], v[134:137], v[102:105], v[66:69]
	global_load_lds_dwordx4 v171, s[30:31] offset:128
	v_mfma_f32_16x16x32_f16 v[42:45], v[138:141], v[102:105], v[42:45]
	v_mfma_f32_16x16x32_f16 v[236:239], v[142:145], v[102:105], v[236:239]
	v_mfma_f32_16x16x32_f16 v[62:65], v[134:137], v[106:109], v[62:65]
	v_mfma_f32_16x16x32_f16 v[38:41], v[138:141], v[106:109], v[38:41]
	v_mfma_f32_16x16x32_f16 v[34:37], v[142:145], v[106:109], v[34:37]
	s_waitcnt vmcnt(6) lgkmcnt(0)
	s_barrier
	s_add_u32 m0, s11, 0x17f00
	ds_read_b128 v[134:137], v162
	global_load_lds_dwordx4 v166, s[28:29] offset:256
	v_mfma_f32_16x16x32_f16 v[82:85], v[146:149], v[110:113], v[82:85]
	ds_read_b128 v[138:141], v162 offset:2048
	v_mfma_f32_16x16x32_f16 v[58:61], v[150:153], v[110:113], v[58:61]
	ds_read_b128 v[142:145], v162 offset:4096
	v_mfma_f32_16x16x32_f16 v[14:17], v[154:157], v[110:113], v[14:17]
	ds_read_b128 v[86:89], v158
	v_mfma_f32_16x16x32_f16 v[78:81], v[146:149], v[114:117], v[78:81]
	ds_read_b128 v[90:93], v158 offset:2048
	v_mfma_f32_16x16x32_f16 v[22:25], v[150:153], v[114:117], v[22:25]
	ds_read_b128 v[94:97], v158 offset:4096
	v_mfma_f32_16x16x32_f16 v[30:33], v[154:157], v[114:117], v[30:33]
	s_add_u32 m0, s11, 0x19f00
	ds_read_b128 v[98:101], v158 offset:6144
	global_load_lds_dwordx4 v167, s[28:29] offset:256
	v_mfma_f32_16x16x32_f16 v[74:77], v[146:149], v[118:121], v[74:77]
	ds_read_b128 v[102:105], v158 offset:8192
	v_mfma_f32_16x16x32_f16 v[18:21], v[150:153], v[118:121], v[18:21]
	ds_read_b128 v[106:109], v158 offset:10240
	v_mfma_f32_16x16x32_f16 v[26:29], v[154:157], v[118:121], v[26:29]
	ds_read_b128 v[110:113], v160
	v_mfma_f32_16x16x32_f16 v[70:73], v[146:149], v[122:125], v[70:73]
	ds_read_b128 v[114:117], v160 offset:2048
	v_mfma_f32_16x16x32_f16 v[46:49], v[150:153], v[122:125], v[46:49]
	v_mfma_f32_16x16x32_f16 v[240:243], v[154:157], v[122:125], v[240:243]
	s_add_u32 m0, s11, 0x1bf00
	ds_read_b128 v[118:121], v160 offset:4096
	global_load_lds_dwordx4 v168, s[28:29] offset:256
	v_mfma_f32_16x16x32_f16 v[66:69], v[146:149], v[126:129], v[66:69]
	ds_read_b128 v[122:125], v160 offset:6144
	v_mfma_f32_16x16x32_f16 v[42:45], v[150:153], v[126:129], v[42:45]
	v_mfma_f32_16x16x32_f16 v[236:239], v[154:157], v[126:129], v[236:239]
	ds_read_b128 v[126:129], v160 offset:8192
	v_mfma_f32_16x16x32_f16 v[62:65], v[146:149], v[130:133], v[62:65]
	v_mfma_f32_16x16x32_f16 v[38:41], v[150:153], v[130:133], v[38:41]
	v_mfma_f32_16x16x32_f16 v[34:37], v[154:157], v[130:133], v[34:37]
	ds_read_b128 v[130:133], v160 offset:10240
	ds_read_b128 v[146:149], v164
	ds_read_b128 v[150:153], v164 offset:2048
	ds_read_b128 v[154:157], v164 offset:4096
	s_add_u32 s28, s28, 0x180
	s_addc_u32 s29, s29, 0
	s_add_u32 s30, s30, 0x180
	s_addc_u32 s31, s31, 0
	s_sub_u32 s22, s22, 1
	s_cmp_lg_u32 s22, 0
	s_cbranch_scc1 .Lgemm_T_loop
	s_waitcnt lgkmcnt(9)
	s_add_u32 m0, s11, 0x1e080
	v_mfma_f32_16x16x32_f16 v[82:85], v[134:137], v[86:89], v[82:85]
	global_load_lds_dwordx4 v169, s[30:31] offset:-128
	v_mfma_f32_16x16x32_f16 v[58:61], v[138:141], v[86:89], v[58:61]
	v_mfma_f32_16x16x32_f16 v[14:17], v[142:145], v[86:89], v[14:17]
	v_mfma_f32_16x16x32_f16 v[78:81], v[134:137], v[90:93], v[78:81]
	v_mfma_f32_16x16x32_f16 v[22:25], v[138:141], v[90:93], v[22:25]
	v_mfma_f32_16x16x32_f16 v[30:33], v[142:145], v[90:93], v[30:33]
	s_add_u32 m0, s11, 0x20080
	v_mfma_f32_16x16x32_f16 v[74:77], v[134:137], v[94:97], v[74:77]
	global_load_lds_dwordx4 v170, s[30:31] offset:-128
	v_mfma_f32_16x16x32_f16 v[18:21], v[138:141], v[94:97], v[18:21]
	v_mfma_f32_16x16x32_f16 v[26:29], v[142:145], v[94:97], v[26:29]
	v_mfma_f32_16x16x32_f16 v[70:73], v[134:137], v[98:101], v[70:73]
	v_mfma_f32_16x16x32_f16 v[46:49], v[138:141], v[98:101], v[46:49]
	v_mfma_f32_16x16x32_f16 v[240:243], v[142:145], v[98:101], v[240:243]
	s_add_u32 m0, s11, 0x22080
	v_mfma_f32_16x16x32_f16 v[66:69], v[134:137], v[102:105], v[66:69]
	global_load_lds_dwordx4 v171, s[30:31] offset:-128
	v_mfma_f32_16x16x32_f16 v[42:45], v[138:141], v[102:105], v[42:45]
	v_mfma_f32_16x16x32_f16 v[236:239], v[142:145], v[102:105], v[236:239]
	v_mfma_f32_16x16x32_f16 v[62:65], v[134:137], v[106:109], v[62:65]
	v_mfma_f32_16x16x32_f16 v[38:41], v[138:141], v[106:109], v[38:41]
	v_mfma_f32_16x16x32_f16 v[34:37], v[142:145], v[106:109], v[34:37]
	s_waitcnt vmcnt(6) lgkmcnt(0)
	s_barrier
	s_add_u32 m0, s11, 0x0
	ds_read_b128 v[134:137], v162 offset:49152
	global_load_lds_dwordx4 v166, s[28:29]
	v_mfma_f32_16x16x32_f16 v[82:85], v[146:149], v[110:113], v[82:85]
	ds_read_b128 v[138:141], v162 offset:51200
	v_mfma_f32_16x16x32_f16 v[58:61], v[150:153], v[110:113], v[58:61]
	ds_read_b128 v[142:145], v162 offset:53248
	v_mfma_f32_16x16x32_f16 v[14:17], v[154:157], v[110:113], v[14:17]
	ds_read_b128 v[86:89], v158 offset:49152
	v_mfma_f32_16x16x32_f16 v[78:81], v[146:149], v[114:117], v[78:81]
	ds_read_b128 v[90:93], v158 offset:51200
	v_mfma_f32_16x16x32_f16 v[22:25], v[150:153], v[114:117], v[22:25]
	ds_read_b128 v[94:97], v158 offset:53248
	v_mfma_f32_16x16x32_f16 v[30:33], v[154:157], v[114:117], v[30:33]
	s_add_u32 m0, s11, 0x2000
	ds_read_b128 v[98:101], v158 offset:55296
	global_load_lds_dwordx4 v167, s[28:29]
	v_mfma_f32_16x16x32_f16 v[74:77], v[146:149], v[118:121], v[74:77]
	ds_read_b128 v[102:105], v158 offset:57344
	v_mfma_f32_16x16x32_f16 v[18:21], v[150:153], v[118:121], v[18:21]
	ds_read_b128 v[106:109], v158 offset:59392
	v_mfma_f32_16x16x32_f16 v[26:29], v[154:157], v[118:121], v[26:29]
	ds_read_b128 v[110:113], v160 offset:49152
	v_mfma_f32_16x16x32_f16 v[70:73], v[146:149], v[122:125], v[70:73]
	ds_read_b128 v[114:117], v160 offset:51200
	v_mfma_f32_16x16x32_f16 v[46:49], v[150:153], v[122:125], v[46:49]
	v_mfma_f32_16x16x32_f16 v[240:243], v[154:157], v[122:125], v[240:243]
	s_add_u32 m0, s11, 0x4000
	ds_read_b128 v[118:121], v160 offset:53248
	global_load_lds_dwordx4 v168, s[28:29]
	v_mfma_f32_16x16x32_f16 v[66:69], v[146:149], v[126:129], v[66:69]
	ds_read_b128 v[122:125], v160 offset:55296
	v_mfma_f32_16x16x32_f16 v[42:45], v[150:153], v[126:129], v[42:45]
	v_mfma_f32_16x16x32_f16 v[236:239], v[154:157], v[126:129], v[236:239]
	ds_read_b128 v[126:129], v160 offset:57344
	v_mfma_f32_16x16x32_f16 v[62:65], v[146:149], v[130:133], v[62:65]
	v_mfma_f32_16x16x32_f16 v[38:41], v[150:153], v[130:133], v[38:41]
	v_mfma_f32_16x16x32_f16 v[34:37], v[154:157], v[130:133], v[34:37]
	ds_read_b128 v[130:133], v160 offset:59392
	ds_read_b128 v[146:149], v164 offset:49152
	ds_read_b128 v[150:153], v164 offset:51200
	ds_read_b128 v[154:157], v164 offset:53248
	s_waitcnt lgkmcnt(9)
	s_add_u32 m0, s11, 0x6000
	v_mfma_f32_16x16x32_f16 v[82:85], v[134:137], v[86:89], v[82:85]
	global_load_lds_dwordx4 v169, s[30:31]
	v_mfma_f32_16x16x32_f16 v[58:61], v[138:141], v[86:89], v[58:61]
	v_mfma_f32_16x16x32_f16 v[14:17], v[142:145], v[86:89], v[14:17]
	v_mfma_f32_16x16x32_f16 v[78:81], v[134:137], v[90:93], v[78:81]
	v_mfma_f32_16x16x32_f16 v[22:25], v[138:141], v[90:93], v[22:25]
	v_mfma_f32_16x16x32_f16 v[30:33], v[142:145], v[90:93], v[30:33]
	s_add_u32 m0, s11, 0x8000
	v_mfma_f32_16x16x32_f16 v[74:77], v[134:137], v[94:97], v[74:77]
	global_load_lds_dwordx4 v170, s[30:31]
	v_mfma_f32_16x16x32_f16 v[18:21], v[138:141], v[94:97], v[18:21]
	v_mfma_f32_16x16x32_f16 v[26:29], v[142:145], v[94:97], v[26:29]
	v_mfma_f32_16x16x32_f16 v[70:73], v[134:137], v[98:101], v[70:73]
	v_mfma_f32_16x16x32_f16 v[46:49], v[138:141], v[98:101], v[46:49]
	v_mfma_f32_16x16x32_f16 v[240:243], v[142:145], v[98:101], v[240:243]
	s_add_u32 m0, s11, 0xa000
	v_mfma_f32_16x16x32_f16 v[66:69], v[134:137], v[102:105], v[66:69]
	global_load_lds_dwordx4 v171, s[30:31]
	v_mfma_f32_16x16x32_f16 v[42:45], v[138:141], v[102:105], v[42:45]
	v_mfma_f32_16x16x32_f16 v[236:239], v[142:145], v[102:105], v[236:239]
	v_mfma_f32_16x16x32_f16 v[62:65], v[134:137], v[106:109], v[62:65]
	v_mfma_f32_16x16x32_f16 v[38:41], v[138:141], v[106:109], v[38:41]
	v_mfma_f32_16x16x32_f16 v[34:37], v[142:145], v[106:109], v[34:37]
	s_waitcnt vmcnt(6) lgkmcnt(0)
	s_barrier
	s_lshl_b32 s26, s17, 2
	s_add_u32 s26, s24, s26
	s_addc_u32 s27, s25, 0
	v_lshlrev_b32_e32 v50, 4, v231
	global_load_dwordx4 v[10:13], v50, s[26:27]
	global_load_dwordx4 v[6:9], v50, s[26:27] offset:64
	global_load_dwordx4 v[2:5], v50, s[26:27] offset:128
	ds_read_b128 v[134:137], v163
	v_mfma_f32_16x16x32_f16 v[82:85], v[146:149], v[110:113], v[82:85]
	ds_read_b128 v[138:141], v163 offset:2048
	v_mfma_f32_16x16x32_f16 v[58:61], v[150:153], v[110:113], v[58:61]
	ds_read_b128 v[142:145], v163 offset:4096
	v_mfma_f32_16x16x32_f16 v[14:17], v[154:157], v[110:113], v[14:17]
	ds_read_b128 v[86:89], v159
	v_mfma_f32_16x16x32_f16 v[78:81], v[146:149], v[114:117], v[78:81]
	ds_read_b128 v[90:93], v159 offset:2048
	v_mfma_f32_16x16x32_f16 v[22:25], v[150:153], v[114:117], v[22:25]
	ds_read_b128 v[94:97], v159 offset:4096
	v_mfma_f32_16x16x32_f16 v[30:33], v[154:157], v[114:117], v[30:33]
	ds_read_b128 v[98:101], v159 offset:6144
	v_mfma_f32_16x16x32_f16 v[74:77], v[146:149], v[118:121], v[74:77]
	ds_read_b128 v[102:105], v159 offset:8192
	v_mfma_f32_16x16x32_f16 v[18:21], v[150:153], v[118:121], v[18:21]
	ds_read_b128 v[106:109], v159 offset:10240
	v_mfma_f32_16x16x32_f16 v[26:29], v[154:157], v[118:121], v[26:29]
	ds_read_b128 v[110:113], v161
	v_mfma_f32_16x16x32_f16 v[70:73], v[146:149], v[122:125], v[70:73]
	ds_read_b128 v[114:117], v161 offset:2048
	v_mfma_f32_16x16x32_f16 v[46:49], v[150:153], v[122:125], v[46:49]
	v_mfma_f32_16x16x32_f16 v[240:243], v[154:157], v[122:125], v[240:243]
	ds_read_b128 v[118:121], v161 offset:4096
	v_mfma_f32_16x16x32_f16 v[66:69], v[146:149], v[126:129], v[66:69]
	ds_read_b128 v[122:125], v161 offset:6144
	v_mfma_f32_16x16x32_f16 v[42:45], v[150:153], v[126:129], v[42:45]
	v_mfma_f32_16x16x32_f16 v[236:239], v[154:157], v[126:129], v[236:239]
	ds_read_b128 v[126:129], v161 offset:8192
	v_mfma_f32_16x16x32_f16 v[62:65], v[146:149], v[130:133], v[62:65]
	v_mfma_f32_16x16x32_f16 v[38:41], v[150:153], v[130:133], v[38:41]
	v_mfma_f32_16x16x32_f16 v[34:37], v[154:157], v[130:133], v[34:37]
	ds_read_b128 v[130:133], v161 offset:10240
	ds_read_b128 v[146:149], v165
	ds_read_b128 v[150:153], v165 offset:2048
	ds_read_b128 v[154:157], v165 offset:4096
	s_waitcnt lgkmcnt(9)
	v_mfma_f32_16x16x32_f16 v[82:85], v[134:137], v[86:89], v[82:85]
	v_mfma_f32_16x16x32_f16 v[58:61], v[138:141], v[86:89], v[58:61]
	v_mfma_f32_16x16x32_f16 v[14:17], v[142:145], v[86:89], v[14:17]
	v_mfma_f32_16x16x32_f16 v[78:81], v[134:137], v[90:93], v[78:81]
	v_mfma_f32_16x16x32_f16 v[22:25], v[138:141], v[90:93], v[22:25]
	v_mfma_f32_16x16x32_f16 v[30:33], v[142:145], v[90:93], v[30:33]
	v_mfma_f32_16x16x32_f16 v[74:77], v[134:137], v[94:97], v[74:77]
	v_mfma_f32_16x16x32_f16 v[18:21], v[138:141], v[94:97], v[18:21]
	v_mfma_f32_16x16x32_f16 v[26:29], v[142:145], v[94:97], v[26:29]
	v_mfma_f32_16x16x32_f16 v[70:73], v[134:137], v[98:101], v[70:73]
	v_mfma_f32_16x16x32_f16 v[46:49], v[138:141], v[98:101], v[46:49]
	v_mfma_f32_16x16x32_f16 v[240:243], v[142:145], v[98:101], v[240:243]
	v_mfma_f32_16x16x32_f16 v[66:69], v[134:137], v[102:105], v[66:69]
	v_mfma_f32_16x16x32_f16 v[42:45], v[138:141], v[102:105], v[42:45]
	v_mfma_f32_16x16x32_f16 v[236:239], v[142:145], v[102:105], v[236:239]
	v_mfma_f32_16x16x32_f16 v[62:65], v[134:137], v[106:109], v[62:65]
	v_mfma_f32_16x16x32_f16 v[38:41], v[138:141], v[106:109], v[38:41]
	v_mfma_f32_16x16x32_f16 v[34:37], v[142:145], v[106:109], v[34:37]
	s_waitcnt vmcnt(3) lgkmcnt(0)
	s_barrier
	ds_read_b128 v[134:137], v162
	v_mfma_f32_16x16x32_f16 v[82:85], v[146:149], v[110:113], v[82:85]
	ds_read_b128 v[138:141], v162 offset:2048
	v_mfma_f32_16x16x32_f16 v[58:61], v[150:153], v[110:113], v[58:61]
	ds_read_b128 v[142:145], v162 offset:4096
	v_mfma_f32_16x16x32_f16 v[14:17], v[154:157], v[110:113], v[14:17]
	ds_read_b128 v[86:89], v158
	v_mfma_f32_16x16x32_f16 v[78:81], v[146:149], v[114:117], v[78:81]
	ds_read_b128 v[90:93], v158 offset:2048
	v_mfma_f32_16x16x32_f16 v[22:25], v[150:153], v[114:117], v[22:25]
	ds_read_b128 v[94:97], v158 offset:4096
	v_mfma_f32_16x16x32_f16 v[30:33], v[154:157], v[114:117], v[30:33]
	ds_read_b128 v[98:101], v158 offset:6144
	v_mfma_f32_16x16x32_f16 v[74:77], v[146:149], v[118:121], v[74:77]
	ds_read_b128 v[102:105], v158 offset:8192
	v_mfma_f32_16x16x32_f16 v[18:21], v[150:153], v[118:121], v[18:21]
	ds_read_b128 v[106:109], v158 offset:10240
	v_mfma_f32_16x16x32_f16 v[26:29], v[154:157], v[118:121], v[26:29]
	ds_read_b128 v[110:113], v160
	v_mfma_f32_16x16x32_f16 v[70:73], v[146:149], v[122:125], v[70:73]
	ds_read_b128 v[114:117], v160 offset:2048
	v_mfma_f32_16x16x32_f16 v[46:49], v[150:153], v[122:125], v[46:49]
	v_mfma_f32_16x16x32_f16 v[240:243], v[154:157], v[122:125], v[240:243]
	ds_read_b128 v[118:121], v160 offset:4096
	v_mfma_f32_16x16x32_f16 v[66:69], v[146:149], v[126:129], v[66:69]
	ds_read_b128 v[122:125], v160 offset:6144
	v_mfma_f32_16x16x32_f16 v[42:45], v[150:153], v[126:129], v[42:45]
	v_mfma_f32_16x16x32_f16 v[236:239], v[154:157], v[126:129], v[236:239]
	ds_read_b128 v[126:129], v160 offset:8192
	v_mfma_f32_16x16x32_f16 v[62:65], v[146:149], v[130:133], v[62:65]
	v_mfma_f32_16x16x32_f16 v[38:41], v[150:153], v[130:133], v[38:41]
	v_mfma_f32_16x16x32_f16 v[34:37], v[154:157], v[130:133], v[34:37]
	ds_read_b128 v[130:133], v160 offset:10240
	ds_read_b128 v[146:149], v164
	ds_read_b128 v[150:153], v164 offset:2048
	ds_read_b128 v[154:157], v164 offset:4096
	s_waitcnt lgkmcnt(9)
	v_mfma_f32_16x16x32_f16 v[82:85], v[134:137], v[86:89], v[82:85]
	v_mfma_f32_16x16x32_f16 v[58:61], v[138:141], v[86:89], v[58:61]
	v_mfma_f32_16x16x32_f16 v[14:17], v[142:145], v[86:89], v[14:17]
	v_mfma_f32_16x16x32_f16 v[78:81], v[134:137], v[90:93], v[78:81]
	v_mfma_f32_16x16x32_f16 v[22:25], v[138:141], v[90:93], v[22:25]
	v_mfma_f32_16x16x32_f16 v[30:33], v[142:145], v[90:93], v[30:33]
	v_mfma_f32_16x16x32_f16 v[74:77], v[134:137], v[94:97], v[74:77]
	v_mfma_f32_16x16x32_f16 v[18:21], v[138:141], v[94:97], v[18:21]
	v_mfma_f32_16x16x32_f16 v[26:29], v[142:145], v[94:97], v[26:29]
	v_mfma_f32_16x16x32_f16 v[70:73], v[134:137], v[98:101], v[70:73]
	v_mfma_f32_16x16x32_f16 v[46:49], v[138:141], v[98:101], v[46:49]
	v_mfma_f32_16x16x32_f16 v[240:243], v[142:145], v[98:101], v[240:243]
	v_mfma_f32_16x16x32_f16 v[66:69], v[134:137], v[102:105], v[66:69]
	v_mfma_f32_16x16x32_f16 v[42:45], v[138:141], v[102:105], v[42:45]
	v_mfma_f32_16x16x32_f16 v[236:239], v[142:145], v[102:105], v[236:239]
	v_mfma_f32_16x16x32_f16 v[62:65], v[134:137], v[106:109], v[62:65]
	v_mfma_f32_16x16x32_f16 v[38:41], v[138:141], v[106:109], v[38:41]
	v_mfma_f32_16x16x32_f16 v[34:37], v[142:145], v[106:109], v[34:37]
	s_waitcnt lgkmcnt(0)
	v_mfma_f32_16x16x32_f16 v[82:85], v[146:149], v[110:113], v[82:85]
	v_mfma_f32_16x16x32_f16 v[58:61], v[150:153], v[110:113], v[58:61]
	v_mfma_f32_16x16x32_f16 v[14:17], v[154:157], v[110:113], v[14:17]
	v_mfma_f32_16x16x32_f16 v[78:81], v[146:149], v[114:117], v[78:81]
	v_mfma_f32_16x16x32_f16 v[22:25], v[150:153], v[114:117], v[22:25]
	v_mfma_f32_16x16x32_f16 v[30:33], v[154:157], v[114:117], v[30:33]
	v_mfma_f32_16x16x32_f16 v[74:77], v[146:149], v[118:121], v[74:77]
	v_mfma_f32_16x16x32_f16 v[18:21], v[150:153], v[118:121], v[18:21]
	v_mfma_f32_16x16x32_f16 v[26:29], v[154:157], v[118:121], v[26:29]
	v_mfma_f32_16x16x32_f16 v[70:73], v[146:149], v[122:125], v[70:73]
	v_mfma_f32_16x16x32_f16 v[46:49], v[150:153], v[122:125], v[46:49]
	v_mfma_f32_16x16x32_f16 v[240:243], v[154:157], v[122:125], v[240:243]
	v_mfma_f32_16x16x32_f16 v[66:69], v[146:149], v[126:129], v[66:69]
	v_mfma_f32_16x16x32_f16 v[42:45], v[150:153], v[126:129], v[42:45]
	v_mfma_f32_16x16x32_f16 v[236:239], v[154:157], v[126:129], v[236:239]
	v_mfma_f32_16x16x32_f16 v[62:65], v[146:149], v[130:133], v[62:65]
	v_mfma_f32_16x16x32_f16 v[38:41], v[150:153], v[130:133], v[38:41]
	v_mfma_f32_16x16x32_f16 v[34:37], v[154:157], v[130:133], v[34:37]
	s_branch .LBB1_76
.Lgemm_N_loop:
	s_waitcnt lgkmcnt(9)
	s_add_u32 m0, s11, 0x1e080
	v_mfma_f32_16x16x32_f16 v[82:85], v[86:89], v[134:137], v[82:85]
	global_load_lds_dwordx4 v169, s[30:31] offset:-128
	v_mfma_f32_16x16x32_f16 v[58:61], v[86:89], v[138:141], v[58:61]
	v_mfma_f32_16x16x32_f16 v[14:17], v[86:89], v[142:145], v[14:17]
	v_mfma_f32_16x16x32_f16 v[78:81], v[90:93], v[134:137], v[78:81]
	v_mfma_f32_16x16x32_f16 v[22:25], v[90:93], v[138:141], v[22:25]
	v_mfma_f32_16x16x32_f16 v[30:33], v[90:93], v[142:145], v[30:33]
	s_add_u32 m0, s11, 0x20080
	v_mfma_f32_16x16x32_f16 v[74:77], v[94:97], v[134:137], v[74:77]
	global_load_lds_dwordx4 v170, s[30:31] offset:-128
	v_mfma_f32_16x16x32_f16 v[18:21], v[94:97], v[138:141], v[18:21]
	v_mfma_f32_16x16x32_f16 v[26:29], v[94:97], v[142:145], v[26:29]
	v_mfma_f32_16x16x32_f16 v[70:73], v[98:101], v[134:137], v[70:73]
	v_mfma_f32_16x16x32_f16 v[46:49], v[98:101], v[138:141], v[46:49]
	v_mfma_f32_16x16x32_f16 v[240:243], v[98:101], v[142:145], v[240:243]
	s_add_u32 m0, s11, 0x22080
	v_mfma_f32_16x16x32_f16 v[66:69], v[102:105], v[134:137], v[66:69]
	global_load_lds_dwordx4 v171, s[30:31] offset:-128
	v_mfma_f32_16x16x32_f16 v[42:45], v[102:105], v[138:141], v[42:45]
	v_mfma_f32_16x16x32_f16 v[236:239], v[102:105], v[142:145], v[236:239]
	v_mfma_f32_16x16x32_f16 v[62:65], v[106:109], v[134:137], v[62:65]
	v_mfma_f32_16x16x32_f16 v[38:41], v[106:109], v[138:141], v[38:41]
	v_mfma_f32_16x16x32_f16 v[34:37], v[106:109], v[142:145], v[34:37]
	s_waitcnt vmcnt(6) lgkmcnt(0)
	s_barrier
	s_add_u32 m0, s11, 0x0
	ds_read_b128 v[134:137], v162 offset:49152
	global_load_lds_dwordx4 v166, s[28:29]
	v_mfma_f32_16x16x32_f16 v[82:85], v[110:113], v[146:149], v[82:85]
	ds_read_b128 v[138:141], v162 offset:51200
	v_mfma_f32_16x16x32_f16 v[58:61], v[110:113], v[150:153], v[58:61]
	ds_read_b128 v[142:145], v162 offset:53248
	v_mfma_f32_16x16x32_f16 v[14:17], v[110:113], v[154:157], v[14:17]
	ds_read_b128 v[86:89], v158 offset:49152
	v_mfma_f32_16x16x32_f16 v[78:81], v[114:117], v[146:149], v[78:81]
	ds_read_b128 v[90:93], v158 offset:51200
	v_mfma_f32_16x16x32_f16 v[22:25], v[114:117], v[150:153], v[22:25]
	ds_read_b128 v[94:97], v158 offset:53248
	v_mfma_f32_16x16x32_f16 v[30:33], v[114:117], v[154:157], v[30:33]
	s_add_u32 m0, s11, 0x2000
	ds_read_b128 v[98:101], v158 offset:55296
	global_load_lds_dwordx4 v167, s[28:29]
	v_mfma_f32_16x16x32_f16 v[74:77], v[118:121], v[146:149], v[74:77]
	ds_read_b128 v[102:105], v158 offset:57344
	v_mfma_f32_16x16x32_f16 v[18:21], v[118:121], v[150:153], v[18:21]
	ds_read_b128 v[106:109], v158 offset:59392
	v_mfma_f32_16x16x32_f16 v[26:29], v[118:121], v[154:157], v[26:29]
	ds_read_b128 v[110:113], v160 offset:49152
	v_mfma_f32_16x16x32_f16 v[70:73], v[122:125], v[146:149], v[70:73]
	ds_read_b128 v[114:117], v160 offset:51200
	v_mfma_f32_16x16x32_f16 v[46:49], v[122:125], v[150:153], v[46:49]
	v_mfma_f32_16x16x32_f16 v[240:243], v[122:125], v[154:157], v[240:243]
	s_add_u32 m0, s11, 0x4000
	ds_read_b128 v[118:121], v160 offset:53248
	global_load_lds_dwordx4 v168, s[28:29]
	v_mfma_f32_16x16x32_f16 v[66:69], v[126:129], v[146:149], v[66:69]
	ds_read_b128 v[122:125], v160 offset:55296
	v_mfma_f32_16x16x32_f16 v[42:45], v[126:129], v[150:153], v[42:45]
	v_mfma_f32_16x16x32_f16 v[236:239], v[126:129], v[154:157], v[236:239]
	ds_read_b128 v[126:129], v160 offset:57344
	v_mfma_f32_16x16x32_f16 v[62:65], v[130:133], v[146:149], v[62:65]
	v_mfma_f32_16x16x32_f16 v[38:41], v[130:133], v[150:153], v[38:41]
	v_mfma_f32_16x16x32_f16 v[34:37], v[130:133], v[154:157], v[34:37]
	ds_read_b128 v[130:133], v160 offset:59392
	ds_read_b128 v[146:149], v164 offset:49152
	ds_read_b128 v[150:153], v164 offset:51200
	ds_read_b128 v[154:157], v164 offset:53248
	s_waitcnt lgkmcnt(9)
	s_add_u32 m0, s11, 0x6000
	v_mfma_f32_16x16x32_f16 v[82:85], v[86:89], v[134:137], v[82:85]
	global_load_lds_dwordx4 v169, s[30:31]
	v_mfma_f32_16x16x32_f16 v[58:61], v[86:89], v[138:141], v[58:61]
	v_mfma_f32_16x16x32_f16 v[14:17], v[86:89], v[142:145], v[14:17]
	v_mfma_f32_16x16x32_f16 v[78:81], v[90:93], v[134:137], v[78:81]
	v_mfma_f32_16x16x32_f16 v[22:25], v[90:93], v[138:141], v[22:25]
	v_mfma_f32_16x16x32_f16 v[30:33], v[90:93], v[142:145], v[30:33]
	s_add_u32 m0, s11, 0x8000
	v_mfma_f32_16x16x32_f16 v[74:77], v[94:97], v[134:137], v[74:77]
	global_load_lds_dwordx4 v170, s[30:31]
	v_mfma_f32_16x16x32_f16 v[18:21], v[94:97], v[138:141], v[18:21]
	v_mfma_f32_16x16x32_f16 v[26:29], v[94:97], v[142:145], v[26:29]
	v_mfma_f32_16x16x32_f16 v[70:73], v[98:101], v[134:137], v[70:73]
	v_mfma_f32_16x16x32_f16 v[46:49], v[98:101], v[138:141], v[46:49]
	v_mfma_f32_16x16x32_f16 v[240:243], v[98:101], v[142:145], v[240:243]
	s_add_u32 m0, s11, 0xa000
	v_mfma_f32_16x16x32_f16 v[66:69], v[102:105], v[134:137], v[66:69]
	global_load_lds_dwordx4 v171, s[30:31]
	v_mfma_f32_16x16x32_f16 v[42:45], v[102:105], v[138:141], v[42:45]
	v_mfma_f32_16x16x32_f16 v[236:239], v[102:105], v[142:145], v[236:239]
	v_mfma_f32_16x16x32_f16 v[62:65], v[106:109], v[134:137], v[62:65]
	v_mfma_f32_16x16x32_f16 v[38:41], v[106:109], v[138:141], v[38:41]
	v_mfma_f32_16x16x32_f16 v[34:37], v[106:109], v[142:145], v[34:37]
	s_waitcnt vmcnt(6) lgkmcnt(0)
	s_barrier
	s_add_u32 m0, s11, 0xbf80
	ds_read_b128 v[134:137], v163
	global_load_lds_dwordx4 v166, s[28:29] offset:128
	v_mfma_f32_16x16x32_f16 v[82:85], v[110:113], v[146:149], v[82:85]
	ds_read_b128 v[138:141], v163 offset:2048
	v_mfma_f32_16x16x32_f16 v[58:61], v[110:113], v[150:153], v[58:61]
	ds_read_b128 v[142:145], v163 offset:4096
	v_mfma_f32_16x16x32_f16 v[14:17], v[110:113], v[154:157], v[14:17]
	ds_read_b128 v[86:89], v159
	v_mfma_f32_16x16x32_f16 v[78:81], v[114:117], v[146:149], v[78:81]
	ds_read_b128 v[90:93], v159 offset:2048
	v_mfma_f32_16x16x32_f16 v[22:25], v[114:117], v[150:153], v[22:25]
	ds_read_b128 v[94:97], v159 offset:4096
	v_mfma_f32_16x16x32_f16 v[30:33], v[114:117], v[154:157], v[30:33]
	s_add_u32 m0, s11, 0xdf80
	ds_read_b128 v[98:101], v159 offset:6144
	global_load_lds_dwordx4 v167, s[28:29] offset:128
	v_mfma_f32_16x16x32_f16 v[74:77], v[118:121], v[146:149], v[74:77]
	ds_read_b128 v[102:105], v159 offset:8192
	v_mfma_f32_16x16x32_f16 v[18:21], v[118:121], v[150:153], v[18:21]
	ds_read_b128 v[106:109], v159 offset:10240
	v_mfma_f32_16x16x32_f16 v[26:29], v[118:121], v[154:157], v[26:29]
	ds_read_b128 v[110:113], v161
	v_mfma_f32_16x16x32_f16 v[70:73], v[122:125], v[146:149], v[70:73]
	ds_read_b128 v[114:117], v161 offset:2048
	v_mfma_f32_16x16x32_f16 v[46:49], v[122:125], v[150:153], v[46:49]
	v_mfma_f32_16x16x32_f16 v[240:243], v[122:125], v[154:157], v[240:243]
	s_add_u32 m0, s11, 0xff80
	ds_read_b128 v[118:121], v161 offset:4096
	global_load_lds_dwordx4 v168, s[28:29] offset:128
	v_mfma_f32_16x16x32_f16 v[66:69], v[126:129], v[146:149], v[66:69]
	ds_read_b128 v[122:125], v161 offset:6144
	v_mfma_f32_16x16x32_f16 v[42:45], v[126:129], v[150:153], v[42:45]
	v_mfma_f32_16x16x32_f16 v[236:239], v[126:129], v[154:157], v[236:239]
	ds_read_b128 v[126:129], v161 offset:8192
	v_mfma_f32_16x16x32_f16 v[62:65], v[130:133], v[146:149], v[62:65]
	v_mfma_f32_16x16x32_f16 v[38:41], v[130:133], v[150:153], v[38:41]
	v_mfma_f32_16x16x32_f16 v[34:37], v[130:133], v[154:157], v[34:37]
	ds_read_b128 v[130:133], v161 offset:10240
	ds_read_b128 v[146:149], v165
	ds_read_b128 v[150:153], v165 offset:2048
	ds_read_b128 v[154:157], v165 offset:4096
	s_waitcnt lgkmcnt(9)
	s_add_u32 m0, s11, 0x11f80
	v_mfma_f32_16x16x32_f16 v[82:85], v[86:89], v[134:137], v[82:85]
	global_load_lds_dwordx4 v169, s[30:31] offset:128
	v_mfma_f32_16x16x32_f16 v[58:61], v[86:89], v[138:141], v[58:61]
	v_mfma_f32_16x16x32_f16 v[14:17], v[86:89], v[142:145], v[14:17]
	v_mfma_f32_16x16x32_f16 v[78:81], v[90:93], v[134:137], v[78:81]
	v_mfma_f32_16x16x32_f16 v[22:25], v[90:93], v[138:141], v[22:25]
	v_mfma_f32_16x16x32_f16 v[30:33], v[90:93], v[142:145], v[30:33]
	s_add_u32 m0, s11, 0x13f80
	v_mfma_f32_16x16x32_f16 v[74:77], v[94:97], v[134:137], v[74:77]
	global_load_lds_dwordx4 v170, s[30:31] offset:128
	v_mfma_f32_16x16x32_f16 v[18:21], v[94:97], v[138:141], v[18:21]
	v_mfma_f32_16x16x32_f16 v[26:29], v[94:97], v[142:145], v[26:29]
	v_mfma_f32_16x16x32_f16 v[70:73], v[98:101], v[134:137], v[70:73]
	v_mfma_f32_16x16x32_f16 v[46:49], v[98:101], v[138:141], v[46:49]
	v_mfma_f32_16x16x32_f16 v[240:243], v[98:101], v[142:145], v[240:243]
	s_add_u32 m0, s11, 0x15f80
	v_mfma_f32_16x16x32_f16 v[66:69], v[102:105], v[134:137], v[66:69]
	global_load_lds_dwordx4 v171, s[30:31] offset:128
	v_mfma_f32_16x16x32_f16 v[42:45], v[102:105], v[138:141], v[42:45]
	v_mfma_f32_16x16x32_f16 v[236:239], v[102:105], v[142:145], v[236:239]
	v_mfma_f32_16x16x32_f16 v[62:65], v[106:109], v[134:137], v[62:65]
	v_mfma_f32_16x16x32_f16 v[38:41], v[106:109], v[138:141], v[38:41]
	v_mfma_f32_16x16x32_f16 v[34:37], v[106:109], v[142:145], v[34:37]
	s_waitcnt vmcnt(6) lgkmcnt(0)
	s_barrier
	s_add_u32 m0, s11, 0x17f00
	ds_read_b128 v[134:137], v162
	global_load_lds_dwordx4 v166, s[28:29] offset:256
	v_mfma_f32_16x16x32_f16 v[82:85], v[110:113], v[146:149], v[82:85]
	ds_read_b128 v[138:141], v162 offset:2048
	v_mfma_f32_16x16x32_f16 v[58:61], v[110:113], v[150:153], v[58:61]
	ds_read_b128 v[142:145], v162 offset:4096
	v_mfma_f32_16x16x32_f16 v[14:17], v[110:113], v[154:157], v[14:17]
	ds_read_b128 v[86:89], v158
	v_mfma_f32_16x16x32_f16 v[78:81], v[114:117], v[146:149], v[78:81]
	ds_read_b128 v[90:93], v158 offset:2048
	v_mfma_f32_16x16x32_f16 v[22:25], v[114:117], v[150:153], v[22:25]
	ds_read_b128 v[94:97], v158 offset:4096
	v_mfma_f32_16x16x32_f16 v[30:33], v[114:117], v[154:157], v[30:33]
	s_add_u32 m0, s11, 0x19f00
	ds_read_b128 v[98:101], v158 offset:6144
	global_load_lds_dwordx4 v167, s[28:29] offset:256
	v_mfma_f32_16x16x32_f16 v[74:77], v[118:121], v[146:149], v[74:77]
	ds_read_b128 v[102:105], v158 offset:8192
	v_mfma_f32_16x16x32_f16 v[18:21], v[118:121], v[150:153], v[18:21]
	ds_read_b128 v[106:109], v158 offset:10240
	v_mfma_f32_16x16x32_f16 v[26:29], v[118:121], v[154:157], v[26:29]
	ds_read_b128 v[110:113], v160
	v_mfma_f32_16x16x32_f16 v[70:73], v[122:125], v[146:149], v[70:73]
	ds_read_b128 v[114:117], v160 offset:2048
	v_mfma_f32_16x16x32_f16 v[46:49], v[122:125], v[150:153], v[46:49]
	v_mfma_f32_16x16x32_f16 v[240:243], v[122:125], v[154:157], v[240:243]
	s_add_u32 m0, s11, 0x1bf00
	ds_read_b128 v[118:121], v160 offset:4096
	global_load_lds_dwordx4 v168, s[28:29] offset:256
	v_mfma_f32_16x16x32_f16 v[66:69], v[126:129], v[146:149], v[66:69]
	ds_read_b128 v[122:125], v160 offset:6144
	v_mfma_f32_16x16x32_f16 v[42:45], v[126:129], v[150:153], v[42:45]
	v_mfma_f32_16x16x32_f16 v[236:239], v[126:129], v[154:157], v[236:239]
	ds_read_b128 v[126:129], v160 offset:8192
	v_mfma_f32_16x16x32_f16 v[62:65], v[130:133], v[146:149], v[62:65]
	v_mfma_f32_16x16x32_f16 v[38:41], v[130:133], v[150:153], v[38:41]
	v_mfma_f32_16x16x32_f16 v[34:37], v[130:133], v[154:157], v[34:37]
	ds_read_b128 v[130:133], v160 offset:10240
	ds_read_b128 v[146:149], v164
	ds_read_b128 v[150:153], v164 offset:2048
	ds_read_b128 v[154:157], v164 offset:4096
	s_add_u32 s28, s28, 0x180
	s_addc_u32 s29, s29, 0
	s_add_u32 s30, s30, 0x180
	s_addc_u32 s31, s31, 0
	s_sub_u32 s22, s22, 1
	s_cmp_lg_u32 s22, 0
	s_cbranch_scc1 .Lgemm_N_loop
	s_waitcnt lgkmcnt(9)
	s_add_u32 m0, s11, 0x1e080
	v_mfma_f32_16x16x32_f16 v[82:85], v[86:89], v[134:137], v[82:85]
	global_load_lds_dwordx4 v169, s[30:31] offset:-128
	v_mfma_f32_16x16x32_f16 v[58:61], v[86:89], v[138:141], v[58:61]
	v_mfma_f32_16x16x32_f16 v[14:17], v[86:89], v[142:145], v[14:17]
	v_mfma_f32_16x16x32_f16 v[78:81], v[90:93], v[134:137], v[78:81]
	v_mfma_f32_16x16x32_f16 v[22:25], v[90:93], v[138:141], v[22:25]
	v_mfma_f32_16x16x32_f16 v[30:33], v[90:93], v[142:145], v[30:33]
	s_add_u32 m0, s11, 0x20080
	v_mfma_f32_16x16x32_f16 v[74:77], v[94:97], v[134:137], v[74:77]
	global_load_lds_dwordx4 v170, s[30:31] offset:-128
	v_mfma_f32_16x16x32_f16 v[18:21], v[94:97], v[138:141], v[18:21]
	v_mfma_f32_16x16x32_f16 v[26:29], v[94:97], v[142:145], v[26:29]
	v_mfma_f32_16x16x32_f16 v[70:73], v[98:101], v[134:137], v[70:73]
	v_mfma_f32_16x16x32_f16 v[46:49], v[98:101], v[138:141], v[46:49]
	v_mfma_f32_16x16x32_f16 v[240:243], v[98:101], v[142:145], v[240:243]
	s_add_u32 m0, s11, 0x22080
	v_mfma_f32_16x16x32_f16 v[66:69], v[102:105], v[134:137], v[66:69]
	global_load_lds_dwordx4 v171, s[30:31] offset:-128
	v_mfma_f32_16x16x32_f16 v[42:45], v[102:105], v[138:141], v[42:45]
	v_mfma_f32_16x16x32_f16 v[236:239], v[102:105], v[142:145], v[236:239]
	v_mfma_f32_16x16x32_f16 v[62:65], v[106:109], v[134:137], v[62:65]
	v_mfma_f32_16x16x32_f16 v[38:41], v[106:109], v[138:141], v[38:41]
	v_mfma_f32_16x16x32_f16 v[34:37], v[106:109], v[142:145], v[34:37]
	s_waitcnt vmcnt(6) lgkmcnt(0)
	s_barrier
	s_add_u32 m0, s11, 0x0
	ds_read_b128 v[134:137], v162 offset:49152
	global_load_lds_dwordx4 v166, s[28:29]
	v_mfma_f32_16x16x32_f16 v[82:85], v[110:113], v[146:149], v[82:85]
	ds_read_b128 v[138:141], v162 offset:51200
	v_mfma_f32_16x16x32_f16 v[58:61], v[110:113], v[150:153], v[58:61]
	ds_read_b128 v[142:145], v162 offset:53248
	v_mfma_f32_16x16x32_f16 v[14:17], v[110:113], v[154:157], v[14:17]
	ds_read_b128 v[86:89], v158 offset:49152
	v_mfma_f32_16x16x32_f16 v[78:81], v[114:117], v[146:149], v[78:81]
	ds_read_b128 v[90:93], v158 offset:51200
	v_mfma_f32_16x16x32_f16 v[22:25], v[114:117], v[150:153], v[22:25]
	ds_read_b128 v[94:97], v158 offset:53248
	v_mfma_f32_16x16x32_f16 v[30:33], v[114:117], v[154:157], v[30:33]
	s_add_u32 m0, s11, 0x2000
	ds_read_b128 v[98:101], v158 offset:55296
	global_load_lds_dwordx4 v167, s[28:29]
	v_mfma_f32_16x16x32_f16 v[74:77], v[118:121], v[146:149], v[74:77]
	ds_read_b128 v[102:105], v158 offset:57344
	v_mfma_f32_16x16x32_f16 v[18:21], v[118:121], v[150:153], v[18:21]
	ds_read_b128 v[106:109], v158 offset:59392
	v_mfma_f32_16x16x32_f16 v[26:29], v[118:121], v[154:157], v[26:29]
	ds_read_b128 v[110:113], v160 offset:49152
	v_mfma_f32_16x16x32_f16 v[70:73], v[122:125], v[146:149], v[70:73]
	ds_read_b128 v[114:117], v160 offset:51200
	v_mfma_f32_16x16x32_f16 v[46:49], v[122:125], v[150:153], v[46:49]
	v_mfma_f32_16x16x32_f16 v[240:243], v[122:125], v[154:157], v[240:243]
	s_add_u32 m0, s11, 0x4000
	ds_read_b128 v[118:121], v160 offset:53248
	global_load_lds_dwordx4 v168, s[28:29]
	v_mfma_f32_16x16x32_f16 v[66:69], v[126:129], v[146:149], v[66:69]
	ds_read_b128 v[122:125], v160 offset:55296
	v_mfma_f32_16x16x32_f16 v[42:45], v[126:129], v[150:153], v[42:45]
	v_mfma_f32_16x16x32_f16 v[236:239], v[126:129], v[154:157], v[236:239]
	ds_read_b128 v[126:129], v160 offset:57344
	v_mfma_f32_16x16x32_f16 v[62:65], v[130:133], v[146:149], v[62:65]
	v_mfma_f32_16x16x32_f16 v[38:41], v[130:133], v[150:153], v[38:41]
	v_mfma_f32_16x16x32_f16 v[34:37], v[130:133], v[154:157], v[34:37]
	ds_read_b128 v[130:133], v160 offset:59392
	ds_read_b128 v[146:149], v164 offset:49152
	ds_read_b128 v[150:153], v164 offset:51200
	ds_read_b128 v[154:157], v164 offset:53248
	s_waitcnt lgkmcnt(9)
	s_add_u32 m0, s11, 0x6000
	v_mfma_f32_16x16x32_f16 v[82:85], v[86:89], v[134:137], v[82:85]
	global_load_lds_dwordx4 v169, s[30:31]
	v_mfma_f32_16x16x32_f16 v[58:61], v[86:89], v[138:141], v[58:61]
	v_mfma_f32_16x16x32_f16 v[14:17], v[86:89], v[142:145], v[14:17]
	v_mfma_f32_16x16x32_f16 v[78:81], v[90:93], v[134:137], v[78:81]
	v_mfma_f32_16x16x32_f16 v[22:25], v[90:93], v[138:141], v[22:25]
	v_mfma_f32_16x16x32_f16 v[30:33], v[90:93], v[142:145], v[30:33]
	s_add_u32 m0, s11, 0x8000
	v_mfma_f32_16x16x32_f16 v[74:77], v[94:97], v[134:137], v[74:77]
	global_load_lds_dwordx4 v170, s[30:31]
	v_mfma_f32_16x16x32_f16 v[18:21], v[94:97], v[138:141], v[18:21]
	v_mfma_f32_16x16x32_f16 v[26:29], v[94:97], v[142:145], v[26:29]
	v_mfma_f32_16x16x32_f16 v[70:73], v[98:101], v[134:137], v[70:73]
	v_mfma_f32_16x16x32_f16 v[46:49], v[98:101], v[138:141], v[46:49]
	v_mfma_f32_16x16x32_f16 v[240:243], v[98:101], v[142:145], v[240:243]
	s_add_u32 m0, s11, 0xa000
	v_mfma_f32_16x16x32_f16 v[66:69], v[102:105], v[134:137], v[66:69]
	global_load_lds_dwordx4 v171, s[30:31]
	v_mfma_f32_16x16x32_f16 v[42:45], v[102:105], v[138:141], v[42:45]
	v_mfma_f32_16x16x32_f16 v[236:239], v[102:105], v[142:145], v[236:239]
	v_mfma_f32_16x16x32_f16 v[62:65], v[106:109], v[134:137], v[62:65]
	v_mfma_f32_16x16x32_f16 v[38:41], v[106:109], v[138:141], v[38:41]
	v_mfma_f32_16x16x32_f16 v[34:37], v[106:109], v[142:145], v[34:37]
	s_waitcnt vmcnt(6) lgkmcnt(0)
	s_barrier
	s_lshl_b32 s26, s17, 2
	s_add_u32 s26, s24, s26
	s_addc_u32 s27, s25, 0
	v_lshlrev_b32_e32 v50, 2, v1
	global_load_dword v234, v50, s[26:27]
	global_load_dword v232, v50, s[26:27] offset:64
	global_load_dword v230, v50, s[26:27] offset:128
	ds_read_b128 v[134:137], v163
	v_mfma_f32_16x16x32_f16 v[82:85], v[110:113], v[146:149], v[82:85]
	ds_read_b128 v[138:141], v163 offset:2048
	v_mfma_f32_16x16x32_f16 v[58:61], v[110:113], v[150:153], v[58:61]
	ds_read_b128 v[142:145], v163 offset:4096
	v_mfma_f32_16x16x32_f16 v[14:17], v[110:113], v[154:157], v[14:17]
	ds_read_b128 v[86:89], v159
	v_mfma_f32_16x16x32_f16 v[78:81], v[114:117], v[146:149], v[78:81]
	ds_read_b128 v[90:93], v159 offset:2048
	v_mfma_f32_16x16x32_f16 v[22:25], v[114:117], v[150:153], v[22:25]
	ds_read_b128 v[94:97], v159 offset:4096
	v_mfma_f32_16x16x32_f16 v[30:33], v[114:117], v[154:157], v[30:33]
	ds_read_b128 v[98:101], v159 offset:6144
	v_mfma_f32_16x16x32_f16 v[74:77], v[118:121], v[146:149], v[74:77]
	ds_read_b128 v[102:105], v159 offset:8192
	v_mfma_f32_16x16x32_f16 v[18:21], v[118:121], v[150:153], v[18:21]
	ds_read_b128 v[106:109], v159 offset:10240
	v_mfma_f32_16x16x32_f16 v[26:29], v[118:121], v[154:157], v[26:29]
	ds_read_b128 v[110:113], v161
	v_mfma_f32_16x16x32_f16 v[70:73], v[122:125], v[146:149], v[70:73]
	ds_read_b128 v[114:117], v161 offset:2048
	v_mfma_f32_16x16x32_f16 v[46:49], v[122:125], v[150:153], v[46:49]
	v_mfma_f32_16x16x32_f16 v[240:243], v[122:125], v[154:157], v[240:243]
	ds_read_b128 v[118:121], v161 offset:4096
	v_mfma_f32_16x16x32_f16 v[66:69], v[126:129], v[146:149], v[66:69]
	ds_read_b128 v[122:125], v161 offset:6144
	v_mfma_f32_16x16x32_f16 v[42:45], v[126:129], v[150:153], v[42:45]
	v_mfma_f32_16x16x32_f16 v[236:239], v[126:129], v[154:157], v[236:239]
	ds_read_b128 v[126:129], v161 offset:8192
	v_mfma_f32_16x16x32_f16 v[62:65], v[130:133], v[146:149], v[62:65]
	v_mfma_f32_16x16x32_f16 v[38:41], v[130:133], v[150:153], v[38:41]
	v_mfma_f32_16x16x32_f16 v[34:37], v[130:133], v[154:157], v[34:37]
	ds_read_b128 v[130:133], v161 offset:10240
	ds_read_b128 v[146:149], v165
	ds_read_b128 v[150:153], v165 offset:2048
	ds_read_b128 v[154:157], v165 offset:4096
	s_waitcnt lgkmcnt(9)
	v_mfma_f32_16x16x32_f16 v[82:85], v[86:89], v[134:137], v[82:85]
	v_mfma_f32_16x16x32_f16 v[58:61], v[86:89], v[138:141], v[58:61]
	v_mfma_f32_16x16x32_f16 v[14:17], v[86:89], v[142:145], v[14:17]
	v_mfma_f32_16x16x32_f16 v[78:81], v[90:93], v[134:137], v[78:81]
	v_mfma_f32_16x16x32_f16 v[22:25], v[90:93], v[138:141], v[22:25]
	v_mfma_f32_16x16x32_f16 v[30:33], v[90:93], v[142:145], v[30:33]
	v_mfma_f32_16x16x32_f16 v[74:77], v[94:97], v[134:137], v[74:77]
	v_mfma_f32_16x16x32_f16 v[18:21], v[94:97], v[138:141], v[18:21]
	v_mfma_f32_16x16x32_f16 v[26:29], v[94:97], v[142:145], v[26:29]
	v_mfma_f32_16x16x32_f16 v[70:73], v[98:101], v[134:137], v[70:73]
	v_mfma_f32_16x16x32_f16 v[46:49], v[98:101], v[138:141], v[46:49]
	v_mfma_f32_16x16x32_f16 v[240:243], v[98:101], v[142:145], v[240:243]
	v_mfma_f32_16x16x32_f16 v[66:69], v[102:105], v[134:137], v[66:69]
	v_mfma_f32_16x16x32_f16 v[42:45], v[102:105], v[138:141], v[42:45]
	v_mfma_f32_16x16x32_f16 v[236:239], v[102:105], v[142:145], v[236:239]
	v_mfma_f32_16x16x32_f16 v[62:65], v[106:109], v[134:137], v[62:65]
	v_mfma_f32_16x16x32_f16 v[38:41], v[106:109], v[138:141], v[38:41]
	v_mfma_f32_16x16x32_f16 v[34:37], v[106:109], v[142:145], v[34:37]
	s_waitcnt vmcnt(3) lgkmcnt(0)
	s_barrier
	ds_read_b128 v[134:137], v162
	v_mfma_f32_16x16x32_f16 v[82:85], v[110:113], v[146:149], v[82:85]
	ds_read_b128 v[138:141], v162 offset:2048
	v_mfma_f32_16x16x32_f16 v[58:61], v[110:113], v[150:153], v[58:61]
	ds_read_b128 v[142:145], v162 offset:4096
	v_mfma_f32_16x16x32_f16 v[14:17], v[110:113], v[154:157], v[14:17]
	ds_read_b128 v[86:89], v158
	v_mfma_f32_16x16x32_f16 v[78:81], v[114:117], v[146:149], v[78:81]
	ds_read_b128 v[90:93], v158 offset:2048
	v_mfma_f32_16x16x32_f16 v[22:25], v[114:117], v[150:153], v[22:25]
	ds_read_b128 v[94:97], v158 offset:4096
	v_mfma_f32_16x16x32_f16 v[30:33], v[114:117], v[154:157], v[30:33]
	ds_read_b128 v[98:101], v158 offset:6144
	v_mfma_f32_16x16x32_f16 v[74:77], v[118:121], v[146:149], v[74:77]
	ds_read_b128 v[102:105], v158 offset:8192
	v_mfma_f32_16x16x32_f16 v[18:21], v[118:121], v[150:153], v[18:21]
	ds_read_b128 v[106:109], v158 offset:10240
	v_mfma_f32_16x16x32_f16 v[26:29], v[118:121], v[154:157], v[26:29]
	ds_read_b128 v[110:113], v160
	v_mfma_f32_16x16x32_f16 v[70:73], v[122:125], v[146:149], v[70:73]
	ds_read_b128 v[114:117], v160 offset:2048
	v_mfma_f32_16x16x32_f16 v[46:49], v[122:125], v[150:153], v[46:49]
	v_mfma_f32_16x16x32_f16 v[240:243], v[122:125], v[154:157], v[240:243]
	ds_read_b128 v[118:121], v160 offset:4096
	v_mfma_f32_16x16x32_f16 v[66:69], v[126:129], v[146:149], v[66:69]
	ds_read_b128 v[122:125], v160 offset:6144
	v_mfma_f32_16x16x32_f16 v[42:45], v[126:129], v[150:153], v[42:45]
	v_mfma_f32_16x16x32_f16 v[236:239], v[126:129], v[154:157], v[236:239]
	ds_read_b128 v[126:129], v160 offset:8192
	v_mfma_f32_16x16x32_f16 v[62:65], v[130:133], v[146:149], v[62:65]
	v_mfma_f32_16x16x32_f16 v[38:41], v[130:133], v[150:153], v[38:41]
	v_mfma_f32_16x16x32_f16 v[34:37], v[130:133], v[154:157], v[34:37]
	ds_read_b128 v[130:133], v160 offset:10240
	ds_read_b128 v[146:149], v164
	ds_read_b128 v[150:153], v164 offset:2048
	ds_read_b128 v[154:157], v164 offset:4096
	s_waitcnt lgkmcnt(9)
	v_mfma_f32_16x16x32_f16 v[82:85], v[86:89], v[134:137], v[82:85]
	v_mfma_f32_16x16x32_f16 v[58:61], v[86:89], v[138:141], v[58:61]
	v_mfma_f32_16x16x32_f16 v[14:17], v[86:89], v[142:145], v[14:17]
	v_mfma_f32_16x16x32_f16 v[78:81], v[90:93], v[134:137], v[78:81]
	v_mfma_f32_16x16x32_f16 v[22:25], v[90:93], v[138:141], v[22:25]
	v_mfma_f32_16x16x32_f16 v[30:33], v[90:93], v[142:145], v[30:33]
	v_mfma_f32_16x16x32_f16 v[74:77], v[94:97], v[134:137], v[74:77]
	v_mfma_f32_16x16x32_f16 v[18:21], v[94:97], v[138:141], v[18:21]
	v_mfma_f32_16x16x32_f16 v[26:29], v[94:97], v[142:145], v[26:29]
	v_mfma_f32_16x16x32_f16 v[70:73], v[98:101], v[134:137], v[70:73]
	v_mfma_f32_16x16x32_f16 v[46:49], v[98:101], v[138:141], v[46:49]
	v_mfma_f32_16x16x32_f16 v[240:243], v[98:101], v[142:145], v[240:243]
	v_mfma_f32_16x16x32_f16 v[66:69], v[102:105], v[134:137], v[66:69]
	v_mfma_f32_16x16x32_f16 v[42:45], v[102:105], v[138:141], v[42:45]
	v_mfma_f32_16x16x32_f16 v[236:239], v[102:105], v[142:145], v[236:239]
	v_mfma_f32_16x16x32_f16 v[62:65], v[106:109], v[134:137], v[62:65]
	v_mfma_f32_16x16x32_f16 v[38:41], v[106:109], v[138:141], v[38:41]
	v_mfma_f32_16x16x32_f16 v[34:37], v[106:109], v[142:145], v[34:37]
	s_waitcnt lgkmcnt(0)
	v_mfma_f32_16x16x32_f16 v[82:85], v[110:113], v[146:149], v[82:85]
	v_mfma_f32_16x16x32_f16 v[58:61], v[110:113], v[150:153], v[58:61]
	v_mfma_f32_16x16x32_f16 v[14:17], v[110:113], v[154:157], v[14:17]
	v_mfma_f32_16x16x32_f16 v[78:81], v[114:117], v[146:149], v[78:81]
	v_mfma_f32_16x16x32_f16 v[22:25], v[114:117], v[150:153], v[22:25]
	v_mfma_f32_16x16x32_f16 v[30:33], v[114:117], v[154:157], v[30:33]
	v_mfma_f32_16x16x32_f16 v[74:77], v[118:121], v[146:149], v[74:77]
	v_mfma_f32_16x16x32_f16 v[18:21], v[118:121], v[150:153], v[18:21]
	v_mfma_f32_16x16x32_f16 v[26:29], v[118:121], v[154:157], v[26:29]
	v_mfma_f32_16x16x32_f16 v[70:73], v[122:125], v[146:149], v[70:73]
	v_mfma_f32_16x16x32_f16 v[46:49], v[122:125], v[150:153], v[46:49]
	v_mfma_f32_16x16x32_f16 v[240:243], v[122:125], v[154:157], v[240:243]
	v_mfma_f32_16x16x32_f16 v[66:69], v[126:129], v[146:149], v[66:69]
	v_mfma_f32_16x16x32_f16 v[42:45], v[126:129], v[150:153], v[42:45]
	v_mfma_f32_16x16x32_f16 v[236:239], v[126:129], v[154:157], v[236:239]
	v_mfma_f32_16x16x32_f16 v[62:65], v[130:133], v[146:149], v[62:65]
	v_mfma_f32_16x16x32_f16 v[38:41], v[130:133], v[150:153], v[38:41]
	v_mfma_f32_16x16x32_f16 v[34:37], v[130:133], v[154:157], v[34:37]
